# grid barrier: follower workgroups issue their agent-scope L1 invalidate (buffer_inv sc1) before spinning on the relay word instead of after release (all waves drained, only sc1 polls in between); repl
# speedup vs baseline: 1.0019x; 1.0019x over previous
.LBB0_207:
	s_or_b64 exec, exec, s[10:11]
	v_cvt_f32_u32_e32 v4, v2
	s_waitcnt vmcnt(0)
	v_readfirstlane_b32 s8, v3
	v_sub_u32_e32 v3, 0, v2
	v_rcp_iflag_f32_e32 v4, v4
	v_add_u32_e32 v5, s8, v1
	v_mul_f32_e32 v4, 0x4f7ffffe, v4
	v_cvt_u32_f32_e32 v4, v4
	v_mul_lo_u32 v1, v3, v4
	v_mul_hi_u32 v1, v4, v1
	v_add_u32_e32 v1, v4, v1
	v_mul_hi_u32 v1, v5, v1
	v_mul_lo_u32 v3, v1, v2
	v_sub_u32_e32 v3, v5, v3
	v_add_u32_e32 v4, 1, v1
	v_cmp_ge_u32_e32 vcc, v3, v2
	s_nop 1
	v_cndmask_b32_e32 v1, v1, v4, vcc
	v_sub_u32_e32 v4, v3, v2
	v_cndmask_b32_e32 v3, v3, v4, vcc
	v_add_u32_e32 v4, 1, v1
	v_cmp_ge_u32_e32 vcc, v3, v2
	v_add_u32_e32 v3, 1, v5
	s_nop 0
	v_cndmask_b32_e32 v1, v1, v4, vcc
	v_mul_lo_u32 v4, v2, v1
	v_add_u32_e32 v2, v4, v2
	v_cmp_ne_u32_e32 vcc, v3, v2
	s_and_saveexec_b64 s[8:9], vcc
	s_xor_b64 s[8:9], exec, s[8:9]
	s_cbranch_execz .LBB0_221
	buffer_inv sc1
	s_waitcnt lgkmcnt(0)
	v_mov_b32_e32 v0, 0x2000
	global_load_dword v0, v0, s[6:7] offset:1024 sc1
	s_add_u32 s14, s6, 0x2400
	s_addc_u32 s15, s7, 0
	s_waitcnt vmcnt(0)
	v_cmp_eq_u32_e32 vcc, v0, v1
	s_and_saveexec_b64 s[10:11], vcc
	s_cbranch_execz .LBB0_220
	s_add_u32 s12, s84, 0x4200
	s_addc_u32 s13, s85, 0
	s_mov_b32 s26, 1
	s_mov_b64 s[16:17], 0
	v_mov_b32_e32 v0, 0
	s_branch .LBB0_211

.LBB0_220:
	s_or_b64 exec, exec, s[10:11]
	s_waitcnt vmcnt(0)
	s_waitcnt vmcnt(0)

.LBB0_295:
	s_or_b64 exec, exec, s[6:7]
	v_cvt_f32_u32_e32 v5, v3
	s_waitcnt vmcnt(0)
	v_readfirstlane_b32 s6, v4
	v_sub_u32_e32 v4, 0, v3
	v_rcp_iflag_f32_e32 v5, v5
	v_add_u32_e32 v6, s6, v0
	v_mul_f32_e32 v5, 0x4f7ffffe, v5
	v_cvt_u32_f32_e32 v5, v5
	v_mul_lo_u32 v0, v4, v5
	v_mul_hi_u32 v0, v5, v0
	v_add_u32_e32 v0, v5, v0
	v_mul_hi_u32 v0, v6, v0
	v_mul_lo_u32 v4, v0, v3
	v_sub_u32_e32 v4, v6, v4
	v_add_u32_e32 v5, 1, v0
	v_cmp_ge_u32_e32 vcc, v4, v3
	s_nop 1
	v_cndmask_b32_e32 v0, v0, v5, vcc
	v_sub_u32_e32 v5, v4, v3
	v_cndmask_b32_e32 v4, v4, v5, vcc
	v_add_u32_e32 v5, 1, v0
	v_cmp_ge_u32_e32 vcc, v4, v3
	v_add_u32_e32 v4, 1, v6
	s_nop 0
	v_cndmask_b32_e32 v0, v0, v5, vcc
	v_mul_lo_u32 v5, v3, v0
	v_add_u32_e32 v3, v5, v3
	v_cmp_ne_u32_e32 vcc, v4, v3
	s_and_saveexec_b64 s[6:7], vcc
	s_xor_b64 s[6:7], exec, s[6:7]
	s_cbranch_execz .LBB0_309
	buffer_inv sc1
	v_readlane_b32 s8, v254, 5
	v_readlane_b32 s9, v254, 6
	s_waitcnt lgkmcnt(0)
	s_nop 3
	global_load_dword v2, v1, s[8:9] sc1
	s_waitcnt vmcnt(0)
	v_cmp_eq_u32_e32 vcc, v2, v0
	s_and_saveexec_b64 s[8:9], vcc
	s_cbranch_execz .LBB0_308
	s_mov_b32 s24, 1
	s_mov_b64 s[10:11], 0
	s_branch .LBB0_299

.LBB0_308:
	s_or_b64 exec, exec, s[8:9]
	s_waitcnt vmcnt(0)
	s_waitcnt vmcnt(0)

.LBB0_1573:
	s_or_b64 exec, exec, s[6:7]
	v_cvt_f32_u32_e32 v5, v3
	s_waitcnt vmcnt(0)
	v_readfirstlane_b32 s6, v4
	v_sub_u32_e32 v4, 0, v3
	v_rcp_iflag_f32_e32 v5, v5
	v_add_u32_e32 v6, s6, v0
	v_mul_f32_e32 v5, 0x4f7ffffe, v5
	v_cvt_u32_f32_e32 v5, v5
	v_mul_lo_u32 v0, v4, v5
	v_mul_hi_u32 v0, v5, v0
	v_add_u32_e32 v0, v5, v0
	v_mul_hi_u32 v0, v6, v0
	v_mul_lo_u32 v4, v0, v3
	v_sub_u32_e32 v4, v6, v4
	v_add_u32_e32 v5, 1, v0
	v_cmp_ge_u32_e32 vcc, v4, v3
	s_nop 1
	v_cndmask_b32_e32 v0, v0, v5, vcc
	v_sub_u32_e32 v5, v4, v3
	v_cndmask_b32_e32 v4, v4, v5, vcc
	v_add_u32_e32 v5, 1, v0
	v_cmp_ge_u32_e32 vcc, v4, v3
	v_add_u32_e32 v4, 1, v6
	s_nop 0
	v_cndmask_b32_e32 v0, v0, v5, vcc
	v_mul_lo_u32 v5, v3, v0
	v_add_u32_e32 v3, v5, v3
	v_cmp_ne_u32_e32 vcc, v4, v3
	s_and_saveexec_b64 s[6:7], vcc
	s_xor_b64 s[6:7], exec, s[6:7]
	s_cbranch_execz .LBB0_1587
	buffer_inv sc1
	v_readlane_b32 s8, v254, 5
	v_readlane_b32 s9, v254, 6
	s_waitcnt lgkmcnt(0)
	s_nop 3
	global_load_dword v2, v1, s[8:9] sc1
	s_waitcnt vmcnt(0)
	v_cmp_eq_u32_e32 vcc, v2, v0
	s_and_saveexec_b64 s[8:9], vcc
	s_cbranch_execz .LBB0_1586
	s_mov_b32 s20, 1
	s_mov_b64 s[10:11], 0
	s_branch .LBB0_1577
